# speedup vs baseline: 1.1055x; 1.0332x over previous
_Z11prep_kernelPKfS0_S0_PcPfS2_S2_S2_:
	s_load_dwordx2 s[2:3], s[0:1], 0x0
	s_load_dwordx4 s[4:7], s[0:1], 0x8
	s_load_dwordx8 s[8:15], s[0:1], 0x18
	s_waitcnt lgkmcnt(0)
	s_branch .Lpp_start
	.p2align 8
.Lpp_start:
	s_mov_b32 s33, s16
	s_mov_b64 s[16:17], s[2:3]
	s_mov_b64 s[18:19], s[4:5]
	s_mov_b64 s[20:21], s[6:7]
	s_mov_b64 s[22:23], s[8:9]
	s_mov_b64 s[24:25], s[10:11]
	s_mov_b64 s[26:27], s[12:13]
	s_mov_b64 s[28:29], s[14:15]
	s_mov_b32 s2, s33
	s_and_b32 s4, s2, 7
	s_lshr_b32 s5, s2, 3
	s_lshl_b32 s6, s4, 4
	s_add_u32 s6, s6, s5
	s_mul_i32 s7, s4, 48
	s_add_u32 s7, s7, s5
	s_add_u32 s7, s7, 0x70
	s_cmp_lt_u32 s5, 16
	s_cselect_b32 s8, s6, s7
	s_lshl_b32 s9, s8, 15
	v_lshrrev_b32_e32 v1, 6, v0
	v_and_b32_e32 v58, 63, v0
	v_lshlrev_b32_e32 v60, 4, v58
	v_readfirstlane_b32 s15, v1
	v_and_b32_e32 v63, 7, v58
	v_lshrrev_b32_e32 v62, 3, v58
	s_lshl_b32 s3, s15, 11
	s_add_u32 s9, s9, s3
	s_waitcnt lgkmcnt(0)
	s_sub_u32 s10, s9, 0x800000
	s_add_u32 s12, s20, s10
	s_addc_u32 s13, s21, 0
	s_mov_b32 s14, 4.0
	s_cmp_lt_u32 s8, 0x100
	s_cbranch_scc0 .Lpp_src
	s_sub_u32 s10, s9, 0x400000
	s_add_u32 s12, s18, s10
	s_addc_u32 s13, s19, 0
	s_cmp_lt_u32 s8, 0x80
	s_cbranch_scc0 .Lpp_src
	s_add_u32 s12, s16, s9
	s_addc_u32 s13, s17, 0
	s_mov_b32 s14, 0x4066d4ca

.Lpp_zout:
	s_load_dwordx2 s[30:31], s[0:1], 0x38
	v_cmp_eq_u32_e32 vcc, 0, v58
	s_and_saveexec_b64 s[6:7], vcc
	s_waitcnt lgkmcnt(0)
	global_store_dword v11, v11, s[30:31]
	s_mov_b64 exec, s[6:7]

	.amdhsa_kernel _Z11prep_kernelPKfS0_S0_PcPfS2_S2_S2_
		.amdhsa_group_segment_fixed_size 36864
		.amdhsa_private_segment_fixed_size 0
		.amdhsa_kernarg_size 64
		.amdhsa_user_sgpr_count 16
		.amdhsa_user_sgpr_dispatch_ptr 0
		.amdhsa_user_sgpr_queue_ptr 0
		.amdhsa_user_sgpr_kernarg_segment_ptr 1
		.amdhsa_user_sgpr_dispatch_id 0
		.amdhsa_user_sgpr_kernarg_preload_length 14
		.amdhsa_user_sgpr_kernarg_preload_offset 0
		.amdhsa_user_sgpr_private_segment_size 0
		.amdhsa_uses_dynamic_stack 0
		.amdhsa_enable_private_segment 0
		.amdhsa_system_sgpr_workgroup_id_x 1
		.amdhsa_system_sgpr_workgroup_id_y 0
		.amdhsa_system_sgpr_workgroup_id_z 0
		.amdhsa_system_sgpr_workgroup_info 0
		.amdhsa_system_vgpr_workitem_id 0
		.amdhsa_next_free_vgpr 64
		.amdhsa_next_free_sgpr 34
		.amdhsa_accum_offset 64
		.amdhsa_reserve_vcc 1
		.amdhsa_float_round_mode_32 0
		.amdhsa_float_round_mode_16_64 0
		.amdhsa_float_denorm_mode_32 3
		.amdhsa_float_denorm_mode_16_64 3
		.amdhsa_dx10_clamp 1
		.amdhsa_ieee_mode 1
		.amdhsa_fp16_overflow 0
		.amdhsa_tg_split 0
		.amdhsa_exception_fp_ieee_invalid_op 0
		.amdhsa_exception_fp_denorm_src 0
		.amdhsa_exception_fp_ieee_div_zero 0
		.amdhsa_exception_fp_ieee_overflow 0
		.amdhsa_exception_fp_ieee_underflow 0
		.amdhsa_exception_fp_ieee_inexact 0
		.amdhsa_exception_int_div_zero 0
	.end_amdhsa_kernel

_Z11main_kernelPKcPfS1_:
	s_load_dwordx2 s[2:3], s[0:1], 0x0
	s_load_dwordx4 s[4:7], s[0:1], 0x8
	s_waitcnt lgkmcnt(0)
	s_branch .Lmk_start
	.p2align 8
.Lmk_start:
	s_mov_b32 s28, s8
	s_mov_b64 s[30:31], s[4:5]
	s_mov_b64 s[32:33], s[6:7]
	s_mov_b64 s[6:7], s[2:3]
	s_mov_b32 s2, s28
	s_and_b32 s3, s2, 7
	s_lshr_b32 s4, s2, 3
	s_and_b32 s5, s4, 3
	s_lshl_b32 s3, s3, 2
	s_or_b32 s8, s3, s5
	s_lshr_b32 s9, s4, 2
	v_lshrrev_b32_e32 v127, 6, v0
	v_and_b32_e32 v124, 63, v0
	v_lshlrev_b32_e32 v124, 4, v124
	v_mov_b32_e32 v120, 0
	v_readfirstlane_b32 s12, v127
	v_mov_b32_e32 v121, 0
	v_mov_b32_e32 v122, 0
	v_mov_b32_e32 v123, 0
	s_lshl_b32 s13, s12, 10
	s_lshl_b32 s14, s9, 3
	s_add_u32 s14, s14, s12
	s_lshl_b32 s15, s14, 13
	s_mul_i32 s16, s8, 0x18000
	s_add_u32 s16, s16, 0x100000
	v_or_b32_e32 v125, s13, v124
	v_or_b32_e32 v126, 0x2000, v125
	s_add_u32 s20, s13, 0x2000
	s_waitcnt lgkmcnt(0)
	s_add_u32 s10, s6, s16
	s_addc_u32 s11, s7, 0
	s_add_u32 s18, s6, s15
	s_addc_u32 s19, s7, 0
	s_add_u32 s22, s18, 0x1000
	s_addc_u32 s23, s19, 0
	s_mov_b32 m0, s13
	s_nop 0
	global_load_lds_dwordx4 v125, s[10:11]
	s_mov_b32 m0, s20
	s_nop 0
	global_load_lds_dwordx4 v126, s[10:11]
	global_load_dwordx4 v[96:99], v124, s[18:19]
	global_load_dwordx2 v[100:101], v124, s[18:19] offset:1024
	global_load_dwordx4 v[102:105], v124, s[18:19] offset:2048
	global_load_dwordx2 v[106:107], v124, s[18:19] offset:3072
	global_load_dwordx4 v[108:111], v124, s[22:23]
	global_load_dwordx2 v[112:113], v124, s[22:23] offset:1024
	global_load_dwordx4 v[114:117], v124, s[22:23] offset:2048
	global_load_dwordx2 v[118:119], v124, s[22:23] offset:3072
	s_add_u32 s24, s10, 0x4000
	s_addc_u32 s25, s11, 0
	s_add_u32 s26, s13, 0x4000
	s_mov_b32 m0, s26
	s_nop 0
	global_load_lds_dwordx4 v125, s[24:25]
	s_add_u32 s26, s20, 0x4000
	s_mov_b32 m0, s26
	s_nop 0
	global_load_lds_dwordx4 v126, s[24:25]
	s_add_u32 s24, s10, 0x8000
	s_addc_u32 s25, s11, 0
	s_add_u32 s26, s13, 0x8000
	s_mov_b32 m0, s26
	s_nop 0
	global_load_lds_dwordx4 v125, s[24:25]
	s_add_u32 s26, s20, 0x8000
	s_mov_b32 m0, s26
	s_nop 0
	global_load_lds_dwordx4 v126, s[24:25]
	s_add_u32 s24, s10, 0xc000
	s_addc_u32 s25, s11, 0
	s_add_u32 s26, s13, 0xc000
	s_mov_b32 m0, s26
	s_nop 0
	global_load_lds_dwordx4 v125, s[24:25]
	s_add_u32 s26, s20, 0xc000
	s_mov_b32 m0, s26
	s_nop 0
	global_load_lds_dwordx4 v126, s[24:25]
	s_waitcnt vmcnt(6)
	s_barrier
	ds_read_b128 v[0:3], v124
	ds_read_b64 v[4:5], v124 offset:1024
	ds_read_b128 v[6:9], v124 offset:2048
	ds_read_b64 v[10:11], v124 offset:3072
	ds_read_b128 v[12:15], v124 offset:4096
	ds_read_b64 v[16:17], v124 offset:5120
	ds_read_b128 v[18:21], v124 offset:6144
	ds_read_b64 v[22:23], v124 offset:7168
	s_waitcnt lgkmcnt(0)
	s_setprio 3
	v_mfma_f32_32x32x64_f8f6f4 v[48:63], v[0:5], v[96:101], 0 cbsz:2 blgp:2
	ds_read_b128 v[24:27], v124 offset:8192
	ds_read_b64 v[28:29], v124 offset:9216
	v_mfma_f32_32x32x64_f8f6f4 v[48:63], v[6:11], v[102:107], v[48:63] cbsz:2 blgp:2
	ds_read_b128 v[30:33], v124 offset:10240
	ds_read_b64 v[34:35], v124 offset:11264
	v_mfma_f32_32x32x64_f8f6f4 v[48:63], v[12:17], v[108:113], v[48:63] cbsz:2 blgp:2
	ds_read_b128 v[36:39], v124 offset:12288
	ds_read_b64 v[40:41], v124 offset:13312
	v_mfma_f32_32x32x64_f8f6f4 v[48:63], v[18:23], v[114:119], v[48:63] cbsz:2 blgp:2
	ds_read_b128 v[42:45], v124 offset:14336
	ds_read_b64 v[46:47], v124 offset:15360
	s_waitcnt vmcnt(4) lgkmcnt(0)
	s_barrier
	s_add_u32 s24, s10, 0x10000
	s_addc_u32 s25, s11, 0
	s_mov_b32 m0, s13
	s_nop 0
	global_load_lds_dwordx4 v125, s[24:25]
	s_mov_b32 m0, s20
	s_nop 0
	global_load_lds_dwordx4 v126, s[24:25]
	v_mfma_f32_32x32x64_f8f6f4 v[64:79], v[24:29], v[96:101], 0 cbsz:2 blgp:2
	ds_read_b128 v[0:3], v124 offset:16384
	ds_read_b64 v[4:5], v124 offset:17408
	ds_read_b128 v[6:9], v124 offset:18432
	ds_read_b64 v[10:11], v124 offset:19456
	ds_read_b128 v[24:27], v124 offset:24576
	ds_read_b64 v[28:29], v124 offset:25600
	v_mfma_f32_32x32x64_f8f6f4 v[64:79], v[30:35], v[102:107], v[64:79] cbsz:2 blgp:2
	ds_read_b128 v[12:15], v124 offset:20480
	ds_read_b64 v[16:17], v124 offset:21504
	ds_read_b128 v[18:21], v124 offset:22528
	ds_read_b64 v[22:23], v124 offset:23552
	ds_read_b128 v[30:33], v124 offset:26624
	ds_read_b64 v[34:35], v124 offset:27648
	v_exp_f32_e32 v48, v48
	v_exp_f32_e32 v49, v49
	v_exp_f32_e32 v50, v50
	v_exp_f32_e32 v51, v51
	v_mfma_f32_32x32x64_f8f6f4 v[64:79], v[36:41], v[108:113], v[64:79] cbsz:2 blgp:2
	ds_read_b128 v[36:39], v124 offset:28672
	ds_read_b64 v[40:41], v124 offset:29696
	v_exp_f32_e32 v52, v52
	v_exp_f32_e32 v53, v53
	v_exp_f32_e32 v54, v54
	v_exp_f32_e32 v55, v55
	v_pk_add_f32 v[120:121], v[120:121], v[48:49]
	v_pk_add_f32 v[122:123], v[122:123], v[50:51]
	v_mfma_f32_32x32x64_f8f6f4 v[64:79], v[42:47], v[114:119], v[64:79] cbsz:2 blgp:2
	ds_read_b128 v[42:45], v124 offset:30720
	ds_read_b64 v[46:47], v124 offset:31744
	v_exp_f32_e32 v56, v56
	v_exp_f32_e32 v57, v57
	v_exp_f32_e32 v58, v58
	v_exp_f32_e32 v59, v59
	v_pk_add_f32 v[120:121], v[120:121], v[52:53]
	v_pk_add_f32 v[122:123], v[122:123], v[54:55]
	s_waitcnt vmcnt(4) lgkmcnt(6)
	s_barrier
	v_mfma_f32_32x32x64_f8f6f4 v[80:95], v[0:5], v[96:101], 0 cbsz:2 blgp:2
	ds_read_b128 v[0:3], v124 offset:32768
	ds_read_b64 v[4:5], v124 offset:33792
	v_exp_f32_e32 v60, v60
	v_exp_f32_e32 v61, v61
	v_exp_f32_e32 v62, v62
	v_exp_f32_e32 v63, v63
	v_pk_add_f32 v[120:121], v[120:121], v[56:57]
	v_pk_add_f32 v[122:123], v[122:123], v[58:59]
	v_mfma_f32_32x32x64_f8f6f4 v[80:95], v[6:11], v[102:107], v[80:95] cbsz:2 blgp:2
	ds_read_b128 v[6:9], v124 offset:34816
	ds_read_b64 v[10:11], v124 offset:35840
	v_exp_f32_e32 v64, v64
	v_exp_f32_e32 v65, v65
	v_exp_f32_e32 v66, v66
	v_exp_f32_e32 v67, v67
	v_pk_add_f32 v[120:121], v[120:121], v[60:61]
	v_pk_add_f32 v[122:123], v[122:123], v[62:63]
	v_mfma_f32_32x32x64_f8f6f4 v[80:95], v[12:17], v[108:113], v[80:95] cbsz:2 blgp:2
	ds_read_b128 v[12:15], v124 offset:36864
	ds_read_b64 v[16:17], v124 offset:37888
	v_exp_f32_e32 v68, v68
	v_exp_f32_e32 v69, v69
	v_exp_f32_e32 v70, v70
	v_exp_f32_e32 v71, v71
	v_pk_add_f32 v[120:121], v[120:121], v[64:65]
	v_pk_add_f32 v[122:123], v[122:123], v[66:67]
	v_mfma_f32_32x32x64_f8f6f4 v[80:95], v[18:23], v[114:119], v[80:95] cbsz:2 blgp:2
	ds_read_b128 v[18:21], v124 offset:38912
	ds_read_b64 v[22:23], v124 offset:39936
	v_exp_f32_e32 v72, v72
	v_exp_f32_e32 v73, v73
	v_exp_f32_e32 v74, v74
	v_exp_f32_e32 v75, v75
	v_pk_add_f32 v[120:121], v[120:121], v[68:69]
	v_pk_add_f32 v[122:123], v[122:123], v[70:71]
	s_waitcnt lgkmcnt(8)
	v_mfma_f32_32x32x64_f8f6f4 v[48:63], v[24:29], v[96:101], 0 cbsz:2 blgp:2
	ds_read_b128 v[24:27], v124 offset:40960
	ds_read_b64 v[28:29], v124 offset:41984
	v_exp_f32_e32 v76, v76
	v_exp_f32_e32 v77, v77
	v_exp_f32_e32 v78, v78
	v_exp_f32_e32 v79, v79
	v_pk_add_f32 v[120:121], v[120:121], v[72:73]
	v_pk_add_f32 v[122:123], v[122:123], v[74:75]
	v_mfma_f32_32x32x64_f8f6f4 v[48:63], v[30:35], v[102:107], v[48:63] cbsz:2 blgp:2
	ds_read_b128 v[30:33], v124 offset:43008
	ds_read_b64 v[34:35], v124 offset:44032
	v_exp_f32_e32 v80, v80
	v_exp_f32_e32 v81, v81
	v_exp_f32_e32 v82, v82
	v_exp_f32_e32 v83, v83
	v_pk_add_f32 v[120:121], v[120:121], v[76:77]
	v_pk_add_f32 v[122:123], v[122:123], v[78:79]
	v_mfma_f32_32x32x64_f8f6f4 v[48:63], v[36:41], v[108:113], v[48:63] cbsz:2 blgp:2
	ds_read_b128 v[36:39], v124 offset:45056
	ds_read_b64 v[40:41], v124 offset:46080
	v_exp_f32_e32 v84, v84
	v_exp_f32_e32 v85, v85
	v_exp_f32_e32 v86, v86
	v_exp_f32_e32 v87, v87
	v_pk_add_f32 v[120:121], v[120:121], v[80:81]
	v_pk_add_f32 v[122:123], v[122:123], v[82:83]
	v_mfma_f32_32x32x64_f8f6f4 v[48:63], v[42:47], v[114:119], v[48:63] cbsz:2 blgp:2
	ds_read_b128 v[42:45], v124 offset:47104
	ds_read_b64 v[46:47], v124 offset:48128
	v_exp_f32_e32 v88, v88
	v_exp_f32_e32 v89, v89
	v_exp_f32_e32 v90, v90
	v_exp_f32_e32 v91, v91
	v_pk_add_f32 v[120:121], v[120:121], v[84:85]
	v_pk_add_f32 v[122:123], v[122:123], v[86:87]
	s_setprio 2
	s_waitcnt vmcnt(2) lgkmcnt(8)
	s_barrier
	s_add_u32 s24, s10, 0x14000
	s_addc_u32 s25, s11, 0
	s_add_u32 s26, s13, 0x4000
	s_mov_b32 m0, s26
	s_nop 0
	global_load_lds_dwordx4 v125, s[24:25]
	s_add_u32 s26, s20, 0x4000
	s_mov_b32 m0, s26
	s_nop 0
	global_load_lds_dwordx4 v126, s[24:25]
	v_mfma_f32_32x32x64_f8f6f4 v[64:79], v[0:5], v[96:101], 0 cbsz:2 blgp:2
	ds_read_b128 v[0:3], v124 offset:49152
	ds_read_b64 v[4:5], v124 offset:50176
	v_exp_f32_e32 v92, v92
	v_exp_f32_e32 v93, v93
	v_exp_f32_e32 v94, v94
	v_exp_f32_e32 v95, v95
	v_pk_add_f32 v[120:121], v[120:121], v[88:89]
	v_pk_add_f32 v[122:123], v[122:123], v[90:91]
	v_mfma_f32_32x32x64_f8f6f4 v[64:79], v[6:11], v[102:107], v[64:79] cbsz:2 blgp:2
	ds_read_b128 v[6:9], v124 offset:51200
	ds_read_b64 v[10:11], v124 offset:52224
	v_exp_f32_e32 v48, v48
	v_exp_f32_e32 v49, v49
	v_exp_f32_e32 v50, v50
	v_exp_f32_e32 v51, v51
	v_pk_add_f32 v[120:121], v[120:121], v[92:93]
	v_pk_add_f32 v[122:123], v[122:123], v[94:95]
	v_mfma_f32_32x32x64_f8f6f4 v[64:79], v[12:17], v[108:113], v[64:79] cbsz:2 blgp:2
	ds_read_b128 v[12:15], v124 offset:53248
	ds_read_b64 v[16:17], v124 offset:54272
	v_exp_f32_e32 v52, v52
	v_exp_f32_e32 v53, v53
	v_exp_f32_e32 v54, v54
	v_exp_f32_e32 v55, v55
	v_pk_add_f32 v[120:121], v[120:121], v[48:49]
	v_pk_add_f32 v[122:123], v[122:123], v[50:51]
	v_mfma_f32_32x32x64_f8f6f4 v[64:79], v[18:23], v[114:119], v[64:79] cbsz:2 blgp:2
	ds_read_b128 v[18:21], v124 offset:55296
	ds_read_b64 v[22:23], v124 offset:56320
	v_exp_f32_e32 v56, v56
	v_exp_f32_e32 v57, v57
	v_exp_f32_e32 v58, v58
	v_exp_f32_e32 v59, v59
	v_pk_add_f32 v[120:121], v[120:121], v[52:53]
	v_pk_add_f32 v[122:123], v[122:123], v[54:55]
	s_waitcnt lgkmcnt(8)
	v_mfma_f32_32x32x64_f8f6f4 v[80:95], v[24:29], v[96:101], 0 cbsz:2 blgp:2
	ds_read_b128 v[24:27], v124 offset:57344
	ds_read_b64 v[28:29], v124 offset:58368
	v_exp_f32_e32 v60, v60
	v_exp_f32_e32 v61, v61
	v_exp_f32_e32 v62, v62
	v_exp_f32_e32 v63, v63
	v_pk_add_f32 v[120:121], v[120:121], v[56:57]
	v_pk_add_f32 v[122:123], v[122:123], v[58:59]
	v_mfma_f32_32x32x64_f8f6f4 v[80:95], v[30:35], v[102:107], v[80:95] cbsz:2 blgp:2
	ds_read_b128 v[30:33], v124 offset:59392
	ds_read_b64 v[34:35], v124 offset:60416
	v_exp_f32_e32 v64, v64
	v_exp_f32_e32 v65, v65
	v_exp_f32_e32 v66, v66
	v_exp_f32_e32 v67, v67
	v_pk_add_f32 v[120:121], v[120:121], v[60:61]
	v_pk_add_f32 v[122:123], v[122:123], v[62:63]
	v_mfma_f32_32x32x64_f8f6f4 v[80:95], v[36:41], v[108:113], v[80:95] cbsz:2 blgp:2
	ds_read_b128 v[36:39], v124 offset:61440
	ds_read_b64 v[40:41], v124 offset:62464
	v_exp_f32_e32 v68, v68
	v_exp_f32_e32 v69, v69
	v_exp_f32_e32 v70, v70
	v_exp_f32_e32 v71, v71
	v_pk_add_f32 v[120:121], v[120:121], v[64:65]
	v_pk_add_f32 v[122:123], v[122:123], v[66:67]
	v_mfma_f32_32x32x64_f8f6f4 v[80:95], v[42:47], v[114:119], v[80:95] cbsz:2 blgp:2
	ds_read_b128 v[42:45], v124 offset:63488
	ds_read_b64 v[46:47], v124 offset:64512
	v_exp_f32_e32 v72, v72
	v_exp_f32_e32 v73, v73
	v_exp_f32_e32 v74, v74
	v_exp_f32_e32 v75, v75
	v_pk_add_f32 v[120:121], v[120:121], v[68:69]
	v_pk_add_f32 v[122:123], v[122:123], v[70:71]
	s_waitcnt vmcnt(2) lgkmcnt(8)
	s_barrier
	v_mfma_f32_32x32x64_f8f6f4 v[48:63], v[0:5], v[96:101], 0 cbsz:2 blgp:2
	ds_read_b128 v[0:3], v124
	ds_read_b64 v[4:5], v124 offset:1024
	v_exp_f32_e32 v76, v76
	v_exp_f32_e32 v77, v77
	v_exp_f32_e32 v78, v78
	v_exp_f32_e32 v79, v79
	v_pk_add_f32 v[120:121], v[120:121], v[72:73]
	v_pk_add_f32 v[122:123], v[122:123], v[74:75]
	v_mfma_f32_32x32x64_f8f6f4 v[48:63], v[6:11], v[102:107], v[48:63] cbsz:2 blgp:2
	ds_read_b128 v[6:9], v124 offset:2048
	ds_read_b64 v[10:11], v124 offset:3072
	v_exp_f32_e32 v80, v80
	v_exp_f32_e32 v81, v81
	v_exp_f32_e32 v82, v82
	v_exp_f32_e32 v83, v83
	v_pk_add_f32 v[120:121], v[120:121], v[76:77]
	v_pk_add_f32 v[122:123], v[122:123], v[78:79]
	v_mfma_f32_32x32x64_f8f6f4 v[48:63], v[12:17], v[108:113], v[48:63] cbsz:2 blgp:2
	ds_read_b128 v[12:15], v124 offset:4096
	ds_read_b64 v[16:17], v124 offset:5120
	v_exp_f32_e32 v84, v84
	v_exp_f32_e32 v85, v85
	v_exp_f32_e32 v86, v86
	v_exp_f32_e32 v87, v87
	v_pk_add_f32 v[120:121], v[120:121], v[80:81]
	v_pk_add_f32 v[122:123], v[122:123], v[82:83]
	v_mfma_f32_32x32x64_f8f6f4 v[48:63], v[18:23], v[114:119], v[48:63] cbsz:2 blgp:2
	ds_read_b128 v[18:21], v124 offset:6144
	ds_read_b64 v[22:23], v124 offset:7168
	v_exp_f32_e32 v88, v88
	v_exp_f32_e32 v89, v89
	v_exp_f32_e32 v90, v90
	v_exp_f32_e32 v91, v91
	v_pk_add_f32 v[120:121], v[120:121], v[84:85]
	v_pk_add_f32 v[122:123], v[122:123], v[86:87]
	s_waitcnt lgkmcnt(8)
	v_mfma_f32_32x32x64_f8f6f4 v[64:79], v[24:29], v[96:101], 0 cbsz:2 blgp:2
	ds_read_b128 v[24:27], v124 offset:8192
	ds_read_b64 v[28:29], v124 offset:9216
	v_exp_f32_e32 v92, v92
	v_exp_f32_e32 v93, v93
	v_exp_f32_e32 v94, v94
	v_exp_f32_e32 v95, v95
	v_pk_add_f32 v[120:121], v[120:121], v[88:89]
	v_pk_add_f32 v[122:123], v[122:123], v[90:91]
	v_mfma_f32_32x32x64_f8f6f4 v[64:79], v[30:35], v[102:107], v[64:79] cbsz:2 blgp:2
	ds_read_b128 v[30:33], v124 offset:10240
	ds_read_b64 v[34:35], v124 offset:11264
	v_exp_f32_e32 v48, v48
	v_exp_f32_e32 v49, v49
	v_exp_f32_e32 v50, v50
	v_exp_f32_e32 v51, v51
	v_pk_add_f32 v[120:121], v[120:121], v[92:93]
	v_pk_add_f32 v[122:123], v[122:123], v[94:95]
	v_mfma_f32_32x32x64_f8f6f4 v[64:79], v[36:41], v[108:113], v[64:79] cbsz:2 blgp:2
	ds_read_b128 v[36:39], v124 offset:12288
	ds_read_b64 v[40:41], v124 offset:13312
	v_exp_f32_e32 v52, v52
	v_exp_f32_e32 v53, v53
	v_exp_f32_e32 v54, v54
	v_exp_f32_e32 v55, v55
	v_pk_add_f32 v[120:121], v[120:121], v[48:49]
	v_pk_add_f32 v[122:123], v[122:123], v[50:51]
	v_mfma_f32_32x32x64_f8f6f4 v[64:79], v[42:47], v[114:119], v[64:79] cbsz:2 blgp:2
	ds_read_b128 v[42:45], v124 offset:14336
	ds_read_b64 v[46:47], v124 offset:15360
	v_exp_f32_e32 v56, v56
	v_exp_f32_e32 v57, v57
	v_exp_f32_e32 v58, v58
	v_exp_f32_e32 v59, v59
	v_pk_add_f32 v[120:121], v[120:121], v[52:53]
	v_pk_add_f32 v[122:123], v[122:123], v[54:55]
	s_setprio 1
	s_waitcnt vmcnt(0) lgkmcnt(8)
	s_barrier
	v_mfma_f32_32x32x64_f8f6f4 v[80:95], v[0:5], v[96:101], 0 cbsz:2 blgp:2
	ds_read_b128 v[0:3], v124 offset:16384
	ds_read_b64 v[4:5], v124 offset:17408
	v_exp_f32_e32 v60, v60
	v_exp_f32_e32 v61, v61
	v_exp_f32_e32 v62, v62
	v_exp_f32_e32 v63, v63
	v_pk_add_f32 v[120:121], v[120:121], v[56:57]
	v_pk_add_f32 v[122:123], v[122:123], v[58:59]
	v_mfma_f32_32x32x64_f8f6f4 v[80:95], v[6:11], v[102:107], v[80:95] cbsz:2 blgp:2
	ds_read_b128 v[6:9], v124 offset:18432
	ds_read_b64 v[10:11], v124 offset:19456
	v_exp_f32_e32 v64, v64
	v_exp_f32_e32 v65, v65
	v_exp_f32_e32 v66, v66
	v_exp_f32_e32 v67, v67
	v_pk_add_f32 v[120:121], v[120:121], v[60:61]
	v_pk_add_f32 v[122:123], v[122:123], v[62:63]
	v_mfma_f32_32x32x64_f8f6f4 v[80:95], v[12:17], v[108:113], v[80:95] cbsz:2 blgp:2
	ds_read_b128 v[12:15], v124 offset:20480
	ds_read_b64 v[16:17], v124 offset:21504
	v_exp_f32_e32 v68, v68
	v_exp_f32_e32 v69, v69
	v_exp_f32_e32 v70, v70
	v_exp_f32_e32 v71, v71
	v_pk_add_f32 v[120:121], v[120:121], v[64:65]
	v_pk_add_f32 v[122:123], v[122:123], v[66:67]
	v_mfma_f32_32x32x64_f8f6f4 v[80:95], v[18:23], v[114:119], v[80:95] cbsz:2 blgp:2
	ds_read_b128 v[18:21], v124 offset:22528
	ds_read_b64 v[22:23], v124 offset:23552
	v_exp_f32_e32 v72, v72
	v_exp_f32_e32 v73, v73
	v_exp_f32_e32 v74, v74
	v_exp_f32_e32 v75, v75
	v_pk_add_f32 v[120:121], v[120:121], v[68:69]
	v_pk_add_f32 v[122:123], v[122:123], v[70:71]
	s_waitcnt lgkmcnt(8)
	v_mfma_f32_32x32x64_f8f6f4 v[48:63], v[24:29], v[96:101], 0 cbsz:2 blgp:2
	ds_read_b128 v[24:27], v124 offset:24576
	ds_read_b64 v[28:29], v124 offset:25600
	v_exp_f32_e32 v76, v76
	v_exp_f32_e32 v77, v77
	v_exp_f32_e32 v78, v78
	v_exp_f32_e32 v79, v79
	v_pk_add_f32 v[120:121], v[120:121], v[72:73]
	v_pk_add_f32 v[122:123], v[122:123], v[74:75]
	v_mfma_f32_32x32x64_f8f6f4 v[48:63], v[30:35], v[102:107], v[48:63] cbsz:2 blgp:2
	ds_read_b128 v[30:33], v124 offset:26624
	ds_read_b64 v[34:35], v124 offset:27648
	v_exp_f32_e32 v80, v80
	v_exp_f32_e32 v81, v81
	v_exp_f32_e32 v82, v82
	v_exp_f32_e32 v83, v83
	v_pk_add_f32 v[120:121], v[120:121], v[76:77]
	v_pk_add_f32 v[122:123], v[122:123], v[78:79]
	s_cmp_lg_u32 s8, 10
	s_cbranch_scc1 .Lmk_nosplit
	v_add_f32_e32 v127, v120, v121
	v_add_f32_e32 v125, v122, v123
	v_mov_b32_e32 v120, 0
	v_mov_b32_e32 v121, 0
	v_mov_b32_e32 v122, 0
	v_mov_b32_e32 v123, 0
	v_add_f32_e32 v127, v127, v125
.Lmk_nosplit:
	v_mfma_f32_32x32x64_f8f6f4 v[48:63], v[36:41], v[108:113], v[48:63] cbsz:2 blgp:2
	ds_read_b128 v[36:39], v124 offset:28672
	ds_read_b64 v[40:41], v124 offset:29696
	v_exp_f32_e32 v84, v84
	v_exp_f32_e32 v85, v85
	v_exp_f32_e32 v86, v86
	v_exp_f32_e32 v87, v87
	v_pk_add_f32 v[120:121], v[120:121], v[80:81]
	v_pk_add_f32 v[122:123], v[122:123], v[82:83]
	v_mfma_f32_32x32x64_f8f6f4 v[48:63], v[42:47], v[114:119], v[48:63] cbsz:2 blgp:2
	ds_read_b128 v[42:45], v124 offset:30720
	ds_read_b64 v[46:47], v124 offset:31744
	v_exp_f32_e32 v88, v88
	v_exp_f32_e32 v89, v89
	v_exp_f32_e32 v90, v90
	v_exp_f32_e32 v91, v91
	v_pk_add_f32 v[120:121], v[120:121], v[84:85]
	v_pk_add_f32 v[122:123], v[122:123], v[86:87]
	s_setprio 0
	s_waitcnt lgkmcnt(8)
	v_mfma_f32_32x32x64_f8f6f4 v[64:79], v[0:5], v[96:101], 0 cbsz:2 blgp:2
	v_exp_f32_e32 v92, v92
	v_exp_f32_e32 v93, v93
	v_exp_f32_e32 v94, v94
	v_exp_f32_e32 v95, v95
	v_pk_add_f32 v[120:121], v[120:121], v[88:89]
	v_pk_add_f32 v[122:123], v[122:123], v[90:91]
	v_mfma_f32_32x32x64_f8f6f4 v[64:79], v[6:11], v[102:107], v[64:79] cbsz:2 blgp:2
	v_exp_f32_e32 v48, v48
	v_exp_f32_e32 v49, v49
	v_exp_f32_e32 v50, v50
	v_exp_f32_e32 v51, v51
	v_pk_add_f32 v[120:121], v[120:121], v[92:93]
	v_pk_add_f32 v[122:123], v[122:123], v[94:95]
	v_mfma_f32_32x32x64_f8f6f4 v[64:79], v[12:17], v[108:113], v[64:79] cbsz:2 blgp:2
	v_exp_f32_e32 v52, v52
	v_exp_f32_e32 v53, v53
	v_exp_f32_e32 v54, v54
	v_exp_f32_e32 v55, v55
	v_pk_add_f32 v[120:121], v[120:121], v[48:49]
	v_pk_add_f32 v[122:123], v[122:123], v[50:51]
	v_mfma_f32_32x32x64_f8f6f4 v[64:79], v[18:23], v[114:119], v[64:79] cbsz:2 blgp:2
	v_exp_f32_e32 v56, v56
	v_exp_f32_e32 v57, v57
	v_exp_f32_e32 v58, v58
	v_exp_f32_e32 v59, v59
	v_pk_add_f32 v[120:121], v[120:121], v[52:53]
	v_pk_add_f32 v[122:123], v[122:123], v[54:55]
	s_waitcnt lgkmcnt(0)
	v_mfma_f32_32x32x64_f8f6f4 v[80:95], v[24:29], v[96:101], 0 cbsz:2 blgp:2
	v_exp_f32_e32 v60, v60
	v_exp_f32_e32 v61, v61
	v_exp_f32_e32 v62, v62
	v_exp_f32_e32 v63, v63
	v_pk_add_f32 v[120:121], v[120:121], v[56:57]
	v_pk_add_f32 v[122:123], v[122:123], v[58:59]
	v_mfma_f32_32x32x64_f8f6f4 v[80:95], v[30:35], v[102:107], v[80:95] cbsz:2 blgp:2
	v_exp_f32_e32 v64, v64
	v_exp_f32_e32 v65, v65
	v_exp_f32_e32 v66, v66
	v_exp_f32_e32 v67, v67
	v_pk_add_f32 v[120:121], v[120:121], v[60:61]
	v_pk_add_f32 v[122:123], v[122:123], v[62:63]
	v_mfma_f32_32x32x64_f8f6f4 v[80:95], v[36:41], v[108:113], v[80:95] cbsz:2 blgp:2
	v_exp_f32_e32 v68, v68
	v_exp_f32_e32 v69, v69
	v_exp_f32_e32 v70, v70
	v_exp_f32_e32 v71, v71
	v_pk_add_f32 v[120:121], v[120:121], v[64:65]
	v_pk_add_f32 v[122:123], v[122:123], v[66:67]
	v_mfma_f32_32x32x64_f8f6f4 v[80:95], v[42:47], v[114:119], v[80:95] cbsz:2 blgp:2
	v_exp_f32_e32 v72, v72
	v_exp_f32_e32 v73, v73
	v_exp_f32_e32 v74, v74
	v_exp_f32_e32 v75, v75
	v_pk_add_f32 v[120:121], v[120:121], v[68:69]
	v_pk_add_f32 v[122:123], v[122:123], v[70:71]
	v_exp_f32_e32 v76, v76
	v_exp_f32_e32 v77, v77
	v_exp_f32_e32 v78, v78
	v_exp_f32_e32 v79, v79
	v_pk_add_f32 v[120:121], v[120:121], v[72:73]
	v_pk_add_f32 v[122:123], v[122:123], v[74:75]
	s_nop 1
	v_exp_f32_e32 v80, v80
	v_exp_f32_e32 v81, v81
	v_exp_f32_e32 v82, v82
	v_exp_f32_e32 v83, v83
	v_pk_add_f32 v[120:121], v[120:121], v[76:77]
	v_pk_add_f32 v[122:123], v[122:123], v[78:79]
	v_exp_f32_e32 v84, v84
	v_exp_f32_e32 v85, v85
	v_exp_f32_e32 v86, v86
	v_exp_f32_e32 v87, v87
	v_pk_add_f32 v[120:121], v[120:121], v[80:81]
	v_pk_add_f32 v[122:123], v[122:123], v[82:83]
	v_exp_f32_e32 v88, v88
	v_exp_f32_e32 v89, v89
	v_exp_f32_e32 v90, v90
	v_exp_f32_e32 v91, v91
	v_pk_add_f32 v[120:121], v[120:121], v[84:85]
	v_pk_add_f32 v[122:123], v[122:123], v[86:87]
	v_exp_f32_e32 v92, v92
	v_exp_f32_e32 v93, v93
	v_exp_f32_e32 v94, v94
	v_exp_f32_e32 v95, v95
	v_pk_add_f32 v[120:121], v[120:121], v[88:89]
	v_pk_add_f32 v[122:123], v[122:123], v[90:91]
	v_pk_add_f32 v[120:121], v[120:121], v[92:93]
	v_pk_add_f32 v[122:123], v[122:123], v[94:95]
	v_add_f32_e32 v120, v120, v121
	v_add_f32_e32 v122, v122, v123
	v_lshrrev_b32_e32 v126, 2, v124
	v_add_f32_e32 v120, v120, v122
	v_xor_b32_e32 v125, 0x80, v126
	s_mov_b64 s[4:5], s[30:31]
	s_mov_b64 s[6:7], s[32:33]
	ds_bpermute_b32 v122, v125, v120
	ds_bpermute_b32 v123, v125, v127
	s_lshl_b32 s14, s14, 7
	v_add_u32_e32 v126, s14, v126
	v_cmp_gt_u32_e32 vcc, 0x200, v124
	s_and_saveexec_b64 s[16:17], vcc
	s_cbranch_execz .Lmk_end
	s_waitcnt lgkmcnt(0)
	v_add_f32_e32 v120, v120, v122
	v_add_f32_e32 v127, v127, v123
	s_cmp_lt_u32 s8, 10
	s_cbranch_scc1 .Lmk_pos_only
	s_cmp_eq_u32 s8, 10
	s_cbranch_scc0 .Lmk_neg_only
	global_atomic_add_f32 v126, v127, s[4:5]

	.amdhsa_kernel _Z11main_kernelPKcPfS1_
		.amdhsa_group_segment_fixed_size 65536
		.amdhsa_private_segment_fixed_size 0
		.amdhsa_kernarg_size 24
		.amdhsa_user_sgpr_count 8
		.amdhsa_user_sgpr_dispatch_ptr 0
		.amdhsa_user_sgpr_queue_ptr 0
		.amdhsa_user_sgpr_kernarg_segment_ptr 1
		.amdhsa_user_sgpr_dispatch_id 0
		.amdhsa_user_sgpr_kernarg_preload_length 6
		.amdhsa_user_sgpr_kernarg_preload_offset 0
		.amdhsa_user_sgpr_private_segment_size 0
		.amdhsa_uses_dynamic_stack 0
		.amdhsa_enable_private_segment 0
		.amdhsa_system_sgpr_workgroup_id_x 1
		.amdhsa_system_sgpr_workgroup_id_y 0
		.amdhsa_system_sgpr_workgroup_id_z 0
		.amdhsa_system_sgpr_workgroup_info 0
		.amdhsa_system_vgpr_workitem_id 0
		.amdhsa_next_free_vgpr 128
		.amdhsa_next_free_sgpr 96
		.amdhsa_accum_offset 128
		.amdhsa_reserve_vcc 1
		.amdhsa_float_round_mode_32 0
		.amdhsa_float_round_mode_16_64 0
		.amdhsa_float_denorm_mode_32 3
		.amdhsa_float_denorm_mode_16_64 3
		.amdhsa_dx10_clamp 1
		.amdhsa_ieee_mode 1
		.amdhsa_fp16_overflow 0
		.amdhsa_tg_split 0
		.amdhsa_exception_fp_ieee_invalid_op 0
		.amdhsa_exception_fp_denorm_src 0
		.amdhsa_exception_fp_ieee_div_zero 0
		.amdhsa_exception_fp_ieee_overflow 0
		.amdhsa_exception_fp_ieee_underflow 0
		.amdhsa_exception_fp_ieee_inexact 0
		.amdhsa_exception_int_div_zero 0
	.end_amdhsa_kernel

_Z12final_kernelPKfS0_S0_S0_Pf:
	s_load_dwordx2 s[2:3], s[0:1], 0x0
	s_load_dwordx4 s[4:7], s[0:1], 0x8
	s_load_dwordx4 s[8:11], s[0:1], 0x18
	s_waitcnt lgkmcnt(0)
	s_branch .Lfk_start
	.p2align 8
.Lfk_start:
	v_and_b32_e32 v1, 15, v0
	v_lshrrev_b32_e32 v2, 4, v0
	v_lshl_or_b32 v3, s12, 8, v0
	v_lshlrev_b32_e32 v3, 2, v3
	v_lshl_or_b32 v1, s12, 4, v1
	v_lshlrev_b32_e32 v1, 2, v1
	v_lshl_or_b32 v2, v2, 13, v1
	v_add_u32_e32 v4, 0x1000, v2
	s_mov_b32 s14, 0x800000
	s_mov_b32 s15, 0x3f317217
	s_mov_b32 s16, 0x7f800000
	v_mov_b32_e32 v18, 0x41b17218
	s_waitcnt lgkmcnt(0)
	global_load_dword v16, v3, s[2:3]
	global_load_dword v17, v3, s[4:5]
	global_load_dword v20, v2, s[6:7]
	global_load_dword v21, v2, s[6:7] offset:1024
	global_load_dword v22, v2, s[6:7] offset:2048
	global_load_dword v23, v2, s[6:7] offset:3072
	global_load_dword v24, v4, s[6:7]
	global_load_dword v25, v4, s[6:7] offset:1024
	global_load_dword v26, v4, s[6:7] offset:2048
	global_load_dword v27, v4, s[6:7] offset:3072
	global_load_dword v28, v2, s[8:9]
	global_load_dword v29, v2, s[8:9] offset:1024
	global_load_dword v30, v2, s[8:9] offset:2048
	global_load_dword v31, v2, s[8:9] offset:3072
	global_load_dword v32, v4, s[8:9]
	global_load_dword v33, v4, s[8:9] offset:1024
	global_load_dword v34, v4, s[8:9] offset:2048
	global_load_dword v35, v4, s[8:9] offset:3072
	v_lshrrev_b32_e32 v9, 6, v0
	v_lshlrev_b32_e32 v9, 2, v9
	v_and_b32_e32 v8, 15, v0
	v_lshl_add_u32 v8, v8, 4, v9
	s_waitcnt vmcnt(16)
	v_add_f32_e32 v14, v16, v17
	v_add_f32_e32 v14, 0x322bcc77, v14
	v_div_scale_f32 v15, s[18:19], v14, v14, v16
	v_rcp_f32_e32 v17, v15
	v_div_scale_f32 v19, vcc, v16, v14, v16
	v_fma_f32 v5, -v15, v17, 1.0
	v_fmac_f32_e32 v17, v5, v17
	v_mul_f32_e32 v5, v19, v17
	v_fma_f32 v6, -v15, v5, v19
	v_fmac_f32_e32 v5, v6, v17
	v_fma_f32 v15, -v15, v5, v19
	v_div_fmas_f32 v15, v15, v17, v5
	v_div_fixup_f32 v14, v15, v14, v16
	v_cmp_gt_f32_e32 vcc, s14, v14
	s_nop 1
	v_cndmask_b32_e64 v15, 0, 32, vcc
	v_ldexp_f32 v14, v14, v15
	v_log_f32_e32 v14, v14
	v_cndmask_b32_e32 v7, 0, v18, vcc
	v_mul_f32_e32 v15, 0x3f317217, v14
	v_fma_f32 v15, v14, s15, -v15
	v_fmamk_f32 v15, v14, 0x3377d1cf, v15
	v_fmac_f32_e32 v15, 0x3f317217, v14
	v_cmp_lt_f32_e64 vcc, |v14|, s16
	s_nop 1
	v_cndmask_b32_e32 v14, v14, v15, vcc
	v_sub_f32_e32 v14, v14, v7
	s_nop 1
	v_add_f32_dpp v14, v14, v14 quad_perm:[1,0,3,2] row_mask:0xf bank_mask:0xf bound_ctrl:1
	s_nop 1
	v_add_f32_dpp v14, v14, v14 quad_perm:[2,3,0,1] row_mask:0xf bank_mask:0xf bound_ctrl:1
	s_nop 1
	v_add_f32_dpp v14, v14, v14 row_half_mirror row_mask:0xf bank_mask:0xf bound_ctrl:1
	s_nop 1
	v_add_f32_dpp v14, v14, v14 row_mirror row_mask:0xf bank_mask:0xf bound_ctrl:1
	s_nop 1
	v_add_f32_dpp v14, v14, v14 row_bcast:15 row_mask:0xa bank_mask:0xf
	s_nop 1
	v_add_f32_dpp v14, v14, v14 row_bcast:31 row_mask:0xc bank_mask:0xf
	s_waitcnt vmcnt(8)
	v_add_f32_e32 v20, v20, v21
	v_add_f32_e32 v22, v22, v23
	v_add_f32_e32 v24, v24, v25
	v_add_f32_e32 v26, v26, v27
	v_add_f32_e32 v20, v20, v22
	v_add_f32_e32 v24, v24, v26
	v_add_f32_e32 v20, v20, v24
	s_waitcnt vmcnt(0)
	v_add_f32_e32 v28, v28, v29
	v_add_f32_e32 v30, v30, v31
	v_add_f32_e32 v32, v32, v33
	v_add_f32_e32 v34, v34, v35
	v_add_f32_e32 v28, v28, v30
	v_add_f32_e32 v32, v32, v34
	v_add_f32_e32 v28, v28, v32
	v_mov_b32_e32 v21, v20
	v_mov_b32_e32 v29, v28
	s_nop 1
	v_permlane16_swap_b32_e32 v20, v21
	v_permlane16_swap_b32_e32 v28, v29
	s_nop 1
	v_add_f32_e32 v20, v20, v21
	v_add_f32_e32 v28, v28, v29
	v_mov_b32_e32 v21, v20
	v_mov_b32_e32 v29, v28
	s_nop 1
	v_permlane32_swap_b32_e32 v20, v21
	v_permlane32_swap_b32_e32 v28, v29
	s_nop 1
	v_add_f32_e32 v20, v20, v21
	v_add_f32_e32 v28, v28, v29
	s_brev_b64 exec, 1
	ds_write_b32 v9, v14
	s_mov_b64 exec, 0xffff
	ds_write_b32 v8, v20 offset:16
	ds_write_b32 v8, v28 offset:272
	s_mov_b64 exec, -1
	s_waitcnt lgkmcnt(0)
	s_barrier
	v_cmp_gt_u32_e32 vcc, 16, v0
	s_and_saveexec_b64 s[14:15], vcc
	s_cbranch_execz .Lfk_end
	v_lshlrev_b32_e32 v1, 4, v0
	v_mov_b32_e32 v2, 0
	ds_read_b128 v[4:7], v1 offset:16
	ds_read_b128 v[10:13], v1 offset:272
	ds_read_b128 v[20:23], v2
	s_cmp_eq_u32 s12, 0
	s_cselect_b32 s3, 0.5, 0
	s_waitcnt lgkmcnt(1)
	v_add_f32_e32 v4, v4, v5
	v_add_f32_e32 v6, v6, v7
	v_add_f32_e32 v10, v10, v11
	v_add_f32_e32 v12, v12, v13
	v_add_f32_e32 v4, v4, v6
	v_add_f32_e32 v10, v10, v12
	v_mul_f32_e32 v4, v4, v10
	s_nop 1
	v_add_f32_dpp v4, v4, v4 quad_perm:[1,0,3,2] row_mask:0xf bank_mask:0xf bound_ctrl:1
	s_nop 1
	v_add_f32_dpp v4, v4, v4 quad_perm:[2,3,0,1] row_mask:0xf bank_mask:0xf bound_ctrl:1
	s_nop 1
	v_add_f32_dpp v4, v4, v4 row_half_mirror row_mask:0xf bank_mask:0xf bound_ctrl:1
	s_nop 1
	v_add_f32_dpp v4, v4, v4 row_mirror row_mask:0xf bank_mask:0xf bound_ctrl:1
	s_nop 1
	s_waitcnt lgkmcnt(0)
	v_add_f32_e32 v20, v20, v21
	v_add_f32_e32 v22, v22, v23
	v_add_f32_e32 v20, v20, v22
	v_mul_f32_e32 v5, 0xb9800000, v20
	v_mul_f32_e32 v6, 0xb10df4e0, v4
	v_add_f32_e32 v5, v5, v6
	v_add_f32_e32 v5, s3, v5
	v_cmp_eq_u32_e32 vcc, 0, v0
	s_and_b64 exec, exec, vcc
	global_atomic_add_f32 v2, v5, s[10:11]

	.amdhsa_kernel _Z12final_kernelPKfS0_S0_S0_Pf
		.amdhsa_group_segment_fixed_size 2064
		.amdhsa_private_segment_fixed_size 0
		.amdhsa_kernarg_size 40
		.amdhsa_user_sgpr_count 12
		.amdhsa_user_sgpr_dispatch_ptr 0
		.amdhsa_user_sgpr_queue_ptr 0
		.amdhsa_user_sgpr_kernarg_segment_ptr 1
		.amdhsa_user_sgpr_dispatch_id 0
		.amdhsa_user_sgpr_kernarg_preload_length 10
		.amdhsa_user_sgpr_kernarg_preload_offset 0
		.amdhsa_user_sgpr_private_segment_size 0
		.amdhsa_uses_dynamic_stack 0
		.amdhsa_enable_private_segment 0
		.amdhsa_system_sgpr_workgroup_id_x 1
		.amdhsa_system_sgpr_workgroup_id_y 0
		.amdhsa_system_sgpr_workgroup_id_z 0
		.amdhsa_system_sgpr_workgroup_info 0
		.amdhsa_system_vgpr_workitem_id 0
		.amdhsa_next_free_vgpr 36
		.amdhsa_next_free_sgpr 20
		.amdhsa_accum_offset 36
		.amdhsa_reserve_vcc 1
		.amdhsa_float_round_mode_32 0
		.amdhsa_float_round_mode_16_64 0
		.amdhsa_float_denorm_mode_32 3
		.amdhsa_float_denorm_mode_16_64 3
		.amdhsa_dx10_clamp 1
		.amdhsa_ieee_mode 1
		.amdhsa_fp16_overflow 0
		.amdhsa_tg_split 0
		.amdhsa_exception_fp_ieee_invalid_op 0
		.amdhsa_exception_fp_denorm_src 0
		.amdhsa_exception_fp_ieee_div_zero 0
		.amdhsa_exception_fp_ieee_overflow 0
		.amdhsa_exception_fp_ieee_underflow 0
		.amdhsa_exception_fp_ieee_inexact 0
		.amdhsa_exception_int_div_zero 0
	.end_amdhsa_kernel
